# P6 consumes act panels in reverse order (most recently written first, still in Infinity Cache) on top of nt loads in P0 P4 P7
# speedup vs baseline: 1.0139x; 1.0070x over previous
;     __device__ __forceinline__ bool next(int i, Unit& u) const {
;         const int U = i * G + vcu, panel = U / NC; if (panel >= npan) return false;
;         const int e = __builtin_amdgcn_readfirstlane((int)pexp[panel]);
;         u.pm = panel; u.pn = U % NC; u.e = e; u.pos0 = (panel - __builtin_amdgcn_readfirstlane(pstart[e])) * 256; u.cnt = __builtin_amdgcn_readfirstlane(cnts[e]); return true;
;     }
; template <class Epi, class Sched>
; __device__ __forceinline__ void gemm_phase(LAS unsigned char* lds, const Sched& S, const Epi& E, const int wid) {
;     ...
;     if (!S.next(0, cur)) return;
.LBB7_854:
	s_or_b64 exec, exec, s[0:1]
	s_ashr_i32 s0, s95, 31
	s_lshr_b32 s0, s0, 30
	s_add_i32 s0, s95, s0
	v_readfirstlane_b32 s2, v1
	s_ashr_i32 s8, s0, 2
	s_cmp_lt_i32 s8, s2
	v_mov_b32_e32 v0, 0
	s_cselect_b64 s[0:1], -1, 0
	s_cmp_ge_i32 s8, s2
	s_waitcnt lgkmcnt(0)
	s_barrier
	s_cbranch_scc1 .LBB7_856
	s_lshl_b32 s101, s8, 2
	s_sub_i32 s101, s95, s101
	s_sub_i32 s8, s2, s8
	s_add_i32 s8, s8, -1
	s_add_i32 s6, s8, 0
	s_add_i32 s6, s6, 0x20340
	v_mov_b32_e32 v1, s6
	ds_read_u8 v1, v1
	s_waitcnt lgkmcnt(0)
	v_readfirstlane_b32 s10, v1
	s_lshl_b32 s6, s10, 2
	s_add_i32 s6, s6, 0
	s_add_i32 s7, s6, 0x20200
	s_add_i32 s6, s6, 0x202a0
	v_mov_b32_e32 v1, s7
	v_mov_b32_e32 v2, s6
	ds_read_b32 v1, v1
	ds_read_b32 v2, v2
	s_mov_b32 s40, s101
	s_ashr_i32 s11, s10, 31
	s_waitcnt lgkmcnt(1)
	v_readfirstlane_b32 s6, v1
	s_sub_i32 s6, s8, s6
	s_waitcnt lgkmcnt(0)
	v_readfirstlane_b32 s19, v2
	s_lshl_b32 s38, s6, 8
	s_andn2_b64 vcc, exec, s[0:1]
	s_cbranch_vccz .LBB7_857
	s_branch .LBB7_928

;     __device__ __forceinline__ bool next(int i, Unit& u) const {
;         const int U = i * G + vcu, panel = U / NC; if (panel >= npan) return false;
;         const int e = __builtin_amdgcn_readfirstlane((int)pexp[panel]);
;         u.pm = panel; u.pn = U % NC; u.e = e; u.pos0 = (panel - __builtin_amdgcn_readfirstlane(pstart[e])) * 256; u.cnt = __builtin_amdgcn_readfirstlane(cnts[e]); return true;
;     }
; template <class Epi, class Sched>
; __device__ __forceinline__ void gemm_phase(LAS unsigned char* lds, const Sched& S, const Epi& E, const int wid) {
;     ...
;         const bool has_next = S.next(ui + 1, nxt);
.LBB7_866:
	s_add_i32 s76, s39, 1
	s_mul_i32 s17, s76, s3
	s_add_i32 s17, s17, s95
	s_ashr_i32 s13, s17, 31
	s_lshr_b32 s13, s13, 30
	s_add_i32 s13, s17, s13
	s_ashr_i32 s13, s13, 2
	s_cmp_lt_i32 s13, s2
	v_mov_b32_e32 v168, 0x43e00000
	s_cselect_b64 s[36:37], -1, 0
	s_cmp_ge_i32 s13, s2
	s_cbranch_scc1 .LBB7_868
	s_lshl_b32 s101, s13, 2
	s_sub_i32 s101, s17, s101
	s_sub_i32 s13, s2, s13
	s_add_i32 s13, s13, -1
	s_add_i32 s12, s13, 0
	s_add_i32 s12, s12, 0x20340
	v_mov_b32_e32 v0, s12
	ds_read_u8 v0, v0
	s_mov_b32 s20, s13
	s_waitcnt lgkmcnt(0)
	v_readfirstlane_b32 s12, v0
	s_lshl_b32 s16, s12, 2
	s_add_i32 s16, s16, 0
	s_add_i32 s18, s16, 0x20200
	s_add_i32 s16, s16, 0x202a0
	v_mov_b32_e32 v0, s18
	v_mov_b32_e32 v1, s16
	ds_read_b32 v0, v0
	ds_read_b32 v1, v1
	s_mov_b32 s16, s101
	s_waitcnt lgkmcnt(1)
	v_readfirstlane_b32 s17, v0
	s_sub_i32 s17, s13, s17
	s_waitcnt lgkmcnt(0)
	v_readfirstlane_b32 s77, v1
	s_lshl_b32 s18, s17, 8

; #define LAS __attribute__((address_space(3)))
; __device__ __forceinline__ int fresh_lane() { unsigned z = 0u; asm volatile("" : "+v"(z)); return (int)__builtin_amdgcn_mbcnt_hi(~0u, __builtin_amdgcn_mbcnt_lo(~0u, z)); }
; __global__ void __launch_bounds__(NWAVES * 64, 2) mk_fwd(Args args) {
;     extern __shared__ __attribute__((aligned(16))) unsigned char lds_raw[];
;     Ctx c; c.pp = &args.p; c.lds = (LAS unsigned char*)lds_raw;
;     c.wave = __builtin_amdgcn_readfirstlane((int)(threadIdx.x >> 6));
;     c.G = gridDim.x; c.bx = blockIdx.x; c.vcu = (c.G % 8 == 0) ? (c.bx % 8) * (c.G / 8) + c.bx / 8 : c.bx;
;     c.ctl = (unsigned*)(args.p.ws + WS_CTL);
;     for (int u = c.wave * 64 + fresh_lane(); u < (LDS_BYTES - LDSCTL_OFF) / 4; u += NWAVES * 64) ((LAS unsigned*)(c.lds + LDSCTL_OFF))[u] = 0u;
	.amdhsa_kernel _Z6mk_fwd4Args
		.amdhsa_group_segment_fixed_size 0
		.amdhsa_private_segment_fixed_size 0
		.amdhsa_kernarg_size 456
		.amdhsa_user_sgpr_count 2
		.amdhsa_user_sgpr_dispatch_ptr 0
		.amdhsa_user_sgpr_queue_ptr 0
		.amdhsa_user_sgpr_kernarg_segment_ptr 1
		.amdhsa_user_sgpr_dispatch_id 0
		.amdhsa_user_sgpr_kernarg_preload_length 0
		.amdhsa_user_sgpr_kernarg_preload_offset 0
		.amdhsa_user_sgpr_private_segment_size 0
		.amdhsa_uses_dynamic_stack 0
		.amdhsa_enable_private_segment 0
		.amdhsa_system_sgpr_workgroup_id_x 1
		.amdhsa_system_sgpr_workgroup_id_y 0
		.amdhsa_system_sgpr_workgroup_id_z 0
		.amdhsa_system_sgpr_workgroup_info 0
		.amdhsa_system_vgpr_workitem_id 0
		.amdhsa_next_free_vgpr 256
		.amdhsa_next_free_sgpr 102
		.amdhsa_accum_offset 256
		.amdhsa_reserve_vcc 1
		.amdhsa_float_round_mode_32 0
		.amdhsa_float_round_mode_16_64 0
		.amdhsa_float_denorm_mode_32 3
		.amdhsa_float_denorm_mode_16_64 3
		.amdhsa_dx10_clamp 1
		.amdhsa_ieee_mode 1
		.amdhsa_fp16_overflow 0
		.amdhsa_tg_split 0
		.amdhsa_exception_fp_ieee_invalid_op 0
		.amdhsa_exception_fp_denorm_src 0
		.amdhsa_exception_fp_ieee_div_zero 0
		.amdhsa_exception_fp_ieee_overflow 0
		.amdhsa_exception_fp_ieee_underflow 0
		.amdhsa_exception_fp_ieee_inexact 0
		.amdhsa_exception_int_div_zero 0
	.end_amdhsa_kernel

; __global__ void k_tables(P p) {
;     float2* cs64 = (float2*)(p.ws + WS_CS64); float2* cs32 = (float2*)(p.ws + WS_CS32);
;     const int i = blockIdx.x * blockDim.x + threadIdx.x;
;     if (i < LPOS * 32) { const int pos = i >> 5, f = i & 31; const float inv = powf(10000.0f, -(float)(2 * f) / 64.0f); const float ang = (float)pos * inv; cs64[i] = make_float2(cosf(ang), sinf(ang)); }
;     if (i < LPOS * 16) { const int pos = i >> 4, f = i & 15; const float inv = powf(10000.0f, -(float)(2 * f) / 32.0f); const float ang = (float)pos * inv; cs32[i] = make_float2(cosf(ang), sinf(ang)); }
;     if (i < 20 * TILE_EL / 2) ((unsigned*)(p.ws + WS_META))[i] = 0u;
; }
; __global__ void k_rstd(P p) {
;     const int row = blockIdx.x * (blockDim.x >> 6) + (threadIdx.x >> 6), lane = threadIdx.x & 63;
;     if (row >= NROWS) return;
;     const float* xr = row < T ? p.x + (size_t)row * DM : p.meta + (size_t)(row - T) * DM;
;     float s = 0.f;
;     for (int j = 0; j < 4; ++j) { const float4 v = ((const float4*)xr)[lane + 64 * j]; s += v.x * v.x + v.y * v.y + v.z * v.z + v.w * v.w; }
;     for (int o = 1; o < 64; o <<= 1) s += __shfl_xor(s, o);
;     if (lane == 0) ((float*)(p.ws + WS_RSTD))[row] = rsqrtf(s * (1.0f / DM) + EPS);
; }
; __global__ __launch_bounds__(256) void k_inproj_naive(P p) {
;     __shared__ float As[16][68], Bs[16][68], Ct[64][65];
;     const int tid = threadIdx.x, tx = tid & 15, ty = tid >> 4, r0 = blockIdx.x * 64, hc = blockIdx.y;
;     const float* rstd = (const float*)(p.ws + WS_RSTD);
;     float acc[4][4] = {};
;     for (int k0 = 0; k0 < DM; k0 += 16) {
;         for (int i = 0; i < 4; ++i) { const int idx = tid + i * 256, rr = idx >> 4, kk = idx & 15, r = r0 + rr; float a = 0.f;
;             if (r < NROWS) { const float* xr = r < T ? p.x + (size_t)r * DM : p.meta + (size_t)(r - T) * DM; a = xr[k0 + kk] * rstd[r] * p.g_attn[k0 + kk]; }
;             As[kk][rr] = a; }
;         for (int i = 0; i < 4; ++i) { const int idx = tid + i * 256, kk = idx >> 6, cc = idx & 63; Bs[kk][cc] = p.w_in[(size_t)(k0 + kk) * INW + hc * 64 + cc]; }
;         __syncthreads();
;         for (int kk = 0; kk < 16; ++kk) { float a[4], bb[4];
;             for (int i = 0; i < 4; ++i) a[i] = As[kk][ty * 4 + i];
;             for (int j = 0; j < 4; ++j) bb[j] = Bs[kk][tx * 4 + j];
amdhsa.kernels:
  - .agpr_count:     0
    .args:
      - .offset:         0
        .size:           192
        .value_kind:     by_value
      - .offset:         192
        .size:           4
        .value_kind:     hidden_block_count_x
      - .offset:         196
        .size:           4
        .value_kind:     hidden_block_count_y
      - .offset:         200
        .size:           4
        .value_kind:     hidden_block_count_z
      - .offset:         204
        .size:           2
        .value_kind:     hidden_group_size_x
      - .offset:         206
        .size:           2
        .value_kind:     hidden_group_size_y
      - .offset:         208
        .size:           2
        .value_kind:     hidden_group_size_z
      - .offset:         210
        .size:           2
        .value_kind:     hidden_remainder_x
      - .offset:         212
        .size:           2
        .value_kind:     hidden_remainder_y
      - .offset:         214
        .size:           2
        .value_kind:     hidden_remainder_z
      - .offset:         232
        .size:           8
        .value_kind:     hidden_global_offset_x
      - .offset:         240
        .size:           8
        .value_kind:     hidden_global_offset_y
      - .offset:         248
        .size:           8
        .value_kind:     hidden_global_offset_z
      - .offset:         256
        .size:           2
        .value_kind:     hidden_grid_dims
    .group_segment_fixed_size: 0
    .kernarg_segment_align: 8
    .kernarg_segment_size: 448
    .language:       OpenCL C
    .language_version:
      - 2
      - 0
    .max_flat_workgroup_size: 1024
    .name:           _Z8k_tables1P
    .private_segment_fixed_size: 0
    .sgpr_count:     20
    .sgpr_spill_count: 0
    .symbol:         _Z8k_tables1P.kd
    .uniform_work_group_size: 1
    .uses_dynamic_stack: false
    .vgpr_count:     22
    .vgpr_spill_count: 0
    .wavefront_size: 64
  - .agpr_count:     0
    .args:
      - .offset:         0
        .size:           192
        .value_kind:     by_value
      - .offset:         192
        .size:           4
        .value_kind:     hidden_block_count_x
      - .offset:         196
        .size:           4
        .value_kind:     hidden_block_count_y
      - .offset:         200
        .size:           4
        .value_kind:     hidden_block_count_z
      - .offset:         204
        .size:           2
        .value_kind:     hidden_group_size_x
      - .offset:         206
        .size:           2
        .value_kind:     hidden_group_size_y
      - .offset:         208
        .size:           2
        .value_kind:     hidden_group_size_z
      - .offset:         210
        .size:           2
        .value_kind:     hidden_remainder_x
      - .offset:         212
        .size:           2
        .value_kind:     hidden_remainder_y
      - .offset:         214
        .size:           2
        .value_kind:     hidden_remainder_z
      - .offset:         232
        .size:           8
        .value_kind:     hidden_global_offset_x
      - .offset:         240
        .size:           8
        .value_kind:     hidden_global_offset_y
      - .offset:         248
        .size:           8
        .value_kind:     hidden_global_offset_z
      - .offset:         256
        .size:           2
        .value_kind:     hidden_grid_dims
    .group_segment_fixed_size: 0
    .kernarg_segment_align: 8
    .kernarg_segment_size: 448
    .language:       OpenCL C
    .language_version:
      - 2
      - 0
    .max_flat_workgroup_size: 1024
    .name:           _Z6k_rstd1P
    .private_segment_fixed_size: 0
    .sgpr_count:     14
    .sgpr_spill_count: 0
    .symbol:         _Z6k_rstd1P.kd
    .uniform_work_group_size: 1
    .uses_dynamic_stack: false
    .vgpr_count:     22
    .vgpr_spill_count: 0
    .wavefront_size: 64
  - .agpr_count:     0
    .args:
      - .offset:         0
        .size:           192
        .value_kind:     by_value
    .group_segment_fixed_size: 25344
    .kernarg_segment_align: 8
    .kernarg_segment_size: 192
    .language:       OpenCL C
    .language_version:
      - 2
      - 0
    .max_flat_workgroup_size: 256
    .name:           _Z14k_inproj_naive1P
    .private_segment_fixed_size: 0
    .sgpr_count:     74
    .sgpr_spill_count: 0
    .symbol:         _Z14k_inproj_naive1P.kd
    .uniform_work_group_size: 1
    .uses_dynamic_stack: false
    .vgpr_count:     118
    .vgpr_spill_count: 0
    .wavefront_size: 64
  - .agpr_count:     0
    .args:
      - .offset:         0
        .size:           192
        .value_kind:     by_value
    .group_segment_fixed_size: 0
    .kernarg_segment_align: 8
    .kernarg_segment_size: 192
    .language:       OpenCL C
    .language_version:
      - 2
      - 0
    .max_flat_workgroup_size: 256
    .name:           _Z11k_swa_naive1P
    .private_segment_fixed_size: 0
    .sgpr_count:     19
    .sgpr_spill_count: 0
    .symbol:         _Z11k_swa_naive1P.kd
    .uniform_work_group_size: 1
    .uses_dynamic_stack: false
    .vgpr_count:     156
    .vgpr_spill_count: 0
    .wavefront_size: 64
; #define LAS __attribute__((address_space(3)))
; __device__ __forceinline__ int fresh_lane() { unsigned z = 0u; asm volatile("" : "+v"(z)); return (int)__builtin_amdgcn_mbcnt_hi(~0u, __builtin_amdgcn_mbcnt_lo(~0u, z)); }
; __device__ __forceinline__ void ph2(const Ctx& c) { att::phase(*c.pp, c.lds + RING_OFF, c.G, c.vcu, c.wave); }
; #define SEAM(k) do { if (IN(k) && IN((k) + 1)) xcd_barrier(bar); } while (0)
; #define PH(k, f) do { if (IN(k)) { f(c); if (PROBE_REP == (k)) { __syncthreads(); f(c); } } } while (0)
; __global__ void __launch_bounds__(NWAVES * 64, 2) mk_fwd(Args args) {
;     extern __shared__ __attribute__((aligned(16))) unsigned char lds_raw[];
;     Ctx c; c.pp = &args.p; c.lds = (LAS unsigned char*)lds_raw;
;     c.wave = __builtin_amdgcn_readfirstlane((int)(threadIdx.x >> 6));
;     c.G = gridDim.x; c.bx = blockIdx.x; c.vcu = (c.G % 8 == 0) ? (c.bx % 8) * (c.G / 8) + c.bx / 8 : c.bx;
;     c.ctl = (unsigned*)(args.p.ws + WS_CTL);
;     for (int u = c.wave * 64 + fresh_lane(); u < (LDS_BYTES - LDSCTL_OFF) / 4; u += NWAVES * 64) ((LAS unsigned*)(c.lds + LDSCTL_OFF))[u] = 0u;
;     __syncthreads();
;     const int lo = args.ph_lo, hi = args.ph_hi;
;     XcdBarrier bar; bar.bar = c.ctl + CW_BAR; bar.x = 0; bar.st = nullptr; bar.wave = c.wave;
;     if (hi - lo > 1) bar = xcd_barrier_post(c.ctl + CW_BAR, (volatile LAS unsigned*)(c.lds + MISC_OFF) + 8, c.wave);
;     ...
;     if (IN(1)) { { pg8::RowOrder S; S.init(T, INW, c.G, c.bx, args.p.ws + WS_MIXED, args.p.ws + WS_WIN); pg8::EpiNull<true> E; pg8::gemm_phase<pg8::EpiNull<true>, pg8::RowOrder>(c.lds + RING_OFF, S, E, c.wave); }
;                  { pg8::RowOrder S; S.init(T, DM, c.G, c.bx, args.p.ws + WS_MIXED, args.p.ws + WS_WOUT); pg8::EpiNull<false> E; pg8::gemm_phase<pg8::EpiNull<false>, pg8::RowOrder>(c.lds + RING_OFF, S, E, c.wave); } __syncthreads(); }
;     ...
;     PH(0, ph0); SEAM(0);
;     PH(1, ph1); SEAM(1);
;     PH(2, ph2); SEAM(2);
;     PH(3, ph3); SEAM(3);
;     PH(4, ph4); SEAM(4);
;     ...
;     if (IN(5)) { ph5null(c); __syncthreads(); }
;     ...
;     if (IN(5)) { ph6null(c); __syncthreads(); }
;     ...
;     PH(5, ph5); SEAM(5);
;     PH(6, ph6); SEAM(6);
;     PH(7, ph7);
;     ...
; }
  - .agpr_count:     0
    .args:
      - .offset:         0
        .size:           192
        .value_kind:     by_value
    .group_segment_fixed_size: 32768
    .kernarg_segment_align: 8
    .kernarg_segment_size: 192
    .language:       OpenCL C
    .language_version:
      - 2
      - 0
    .max_flat_workgroup_size: 256
    .name:           _Z12k_diff_naive1P
    .private_segment_fixed_size: 0
    .sgpr_count:     90
    .sgpr_spill_count: 0
    .symbol:         _Z12k_diff_naive1P.kd
    .uniform_work_group_size: 1
    .uses_dynamic_stack: false
    .vgpr_count:     252
    .vgpr_spill_count: 0
    .wavefront_size: 64
  - .agpr_count:     0
    .args:
      - .offset:         0
        .size:           192
        .value_kind:     by_value
      - .offset:         192
        .size:           4
        .value_kind:     hidden_block_count_x
      - .offset:         196
        .size:           4
        .value_kind:     hidden_block_count_y
      - .offset:         200
        .size:           4
        .value_kind:     hidden_block_count_z
      - .offset:         204
        .size:           2
        .value_kind:     hidden_group_size_x
      - .offset:         206
        .size:           2
        .value_kind:     hidden_group_size_y
      - .offset:         208
        .size:           2
        .value_kind:     hidden_group_size_z
      - .offset:         210
        .size:           2
        .value_kind:     hidden_remainder_x
      - .offset:         212
        .size:           2
        .value_kind:     hidden_remainder_y
      - .offset:         214
        .size:           2
        .value_kind:     hidden_remainder_z
      - .offset:         232
        .size:           8
        .value_kind:     hidden_global_offset_x
      - .offset:         240
        .size:           8
        .value_kind:     hidden_global_offset_y
      - .offset:         248
        .size:           8
        .value_kind:     hidden_global_offset_z
      - .offset:         256
        .size:           2
        .value_kind:     hidden_grid_dims
    .group_segment_fixed_size: 18688
    .kernarg_segment_align: 8
    .kernarg_segment_size: 448
    .language:       OpenCL C
    .language_version:
      - 2
      - 0
    .max_flat_workgroup_size: 256
    .name:           _Z7k_route1P
    .private_segment_fixed_size: 0
    .sgpr_count:     35
    .sgpr_spill_count: 0
    .symbol:         _Z7k_route1P.kd
    .uniform_work_group_size: 1
    .uses_dynamic_stack: false
    .vgpr_count:     62
    .vgpr_spill_count: 0
    .wavefront_size: 64
  - .agpr_count:     0
    .args:
      - .offset:         0
        .size:           192
        .value_kind:     by_value
    .group_segment_fixed_size: 0
    .kernarg_segment_align: 8
    .kernarg_segment_size: 192
    .language:       OpenCL C
    .language_version:
      - 2
      - 0
    .max_flat_workgroup_size: 256
    .name:           _Z9k_combine1P
    .private_segment_fixed_size: 0
    .sgpr_count:     14
    .sgpr_spill_count: 0
    .symbol:         _Z9k_combine1P.kd
    .uniform_work_group_size: 1
    .uses_dynamic_stack: false
    .vgpr_count:     20
    .vgpr_spill_count: 0
    .wavefront_size: 64
  - .agpr_count:     0
    .args:
      - .offset:         0
        .size:           200
        .value_kind:     by_value
      - .offset:         200
        .size:           4
        .value_kind:     hidden_block_count_x
      - .offset:         204
        .size:           4
        .value_kind:     hidden_block_count_y
      - .offset:         208
        .size:           4
        .value_kind:     hidden_block_count_z
      - .offset:         212
        .size:           2
        .value_kind:     hidden_group_size_x
      - .offset:         214
        .size:           2
        .value_kind:     hidden_group_size_y
      - .offset:         216
        .size:           2
        .value_kind:     hidden_group_size_z
      - .offset:         218
        .size:           2
        .value_kind:     hidden_remainder_x
      - .offset:         220
        .size:           2
        .value_kind:     hidden_remainder_y
      - .offset:         222
        .size:           2
        .value_kind:     hidden_remainder_z
      - .offset:         240
        .size:           8
        .value_kind:     hidden_global_offset_x
      - .offset:         248
        .size:           8
        .value_kind:     hidden_global_offset_y
      - .offset:         256
        .size:           8
        .value_kind:     hidden_global_offset_z
      - .offset:         264
        .size:           2
        .value_kind:     hidden_grid_dims
      - .offset:         320
        .size:           4
        .value_kind:     hidden_dynamic_lds_size
    .group_segment_fixed_size: 0
    .kernarg_segment_align: 8
    .kernarg_segment_size: 456
    .language:       OpenCL C
    .language_version:
      - 2
      - 0
    .max_flat_workgroup_size: 512
    .name:           _Z6mk_fwd4Args
    .private_segment_fixed_size: 0
    .sgpr_count:     108
    .sgpr_spill_count: 94
    .symbol:         _Z6mk_fwd4Args.kd
    .uniform_work_group_size: 1
    .uses_dynamic_stack: false
    .vgpr_count:     256
    .vgpr_spill_count: 0
    .wavefront_size: 64
